# v61 + P5 epilogue: SwiGLU bias fragment loads issued one K tile earlier (tile waits +4), no exposed round trip at the epilogue head
# speedup vs baseline: 1.0114x; 1.0043x over previous
.LBB0_648:
	s_mov_b32 m0, s85
	ds_read_b64_tr_b16 v[198:199], v187
	ds_read_b64_tr_b16 v[180:181], v187 offset:32
	ds_read_b64_tr_b16 v[202:203], v187 offset:64
	ds_read_b64_tr_b16 v[176:177], v187 offset:96
	ds_read_b64_tr_b16 v[200:201], v188
	ds_read_b64_tr_b16 v[182:183], v188 offset:32
	ds_read_b64_tr_b16 v[204:205], v188 offset:64
	ds_read_b64_tr_b16 v[178:179], v188 offset:96
	ds_read_b128 v[206:209], v186
	ds_read_b128 v[210:213], v186 offset:2048
	ds_read_b128 v[214:217], v186 offset:4096
	buffer_load_dwordx4 v189, s[20:23], s49 offen lds
	s_mov_b32 m0, s7
	s_add_i32 s16, s65, -1
	buffer_load_dwordx4 v192, s[20:23], s49 offen lds
	s_mov_b32 m0, s6
	s_and_b32 s25, s67, 0xffff
	buffer_load_dwordx4 v191, s[20:23], s49 offen lds
	s_mov_b32 m0, s47
	s_mov_b32 s24, s66
	buffer_load_dwordx4 v190, s[20:23], s49 offen lds
	s_mov_b32 m0, s48
	s_mov_b32 s26, s18
	buffer_load_dwordx4 v193, s[20:23], s49 offen lds
	v_mbcnt_lo_u32_b32 v189, -1, 0
	v_mbcnt_hi_u32_b32 v189, -1, v189
	s_mov_b32 s27, s19
	v_ashrrev_i32_e32 v190, 2, v189
	v_add_u32_e32 v190, s78, v190
	v_add_u32_e32 v191, s81, v190
	v_min_i32_e32 v192, s16, v191
	v_add_u32_e32 v193, 64, v191
	v_add_u32_e32 v195, 0x80, v191
	v_add_u32_e32 v191, 0xc0, v191
	v_add_u32_e32 v190, s82, v190
	v_min_i32_e32 v193, s16, v193
	v_min_i32_e32 v195, s16, v195
	v_min_i32_e32 v191, s16, v191
	v_min_i32_e32 v190, s16, v190
	v_lshlrev_b32_e32 v192, 2, v192
	v_lshlrev_b32_e32 v193, 2, v193
	v_lshlrev_b32_e32 v195, 2, v195
	v_lshlrev_b32_e32 v191, 2, v191
	v_lshlrev_b32_e32 v190, 2, v190
	buffer_load_dword v192, v192, s[24:27], 0 offen
	s_nop 0
	buffer_load_dword v193, v193, s[24:27], 0 offen
	s_nop 0
	buffer_load_dword v195, v195, s[24:27], 0 offen
	s_nop 0
	buffer_load_dword v191, v191, s[24:27], 0 offen
	s_nop 0
	buffer_load_dword v190, v190, s[24:27], 0 offen
	v_lshlrev_b32_e32 v197, 4, v189
	v_and_b32_e32 v189, 32, v189
	v_and_b32_e32 v197, 48, v197
	v_bitop3_b32 v197, v197, s84, v189 bitop3:0xde
	s_and_b32 s25, s77, 0xffff
	s_mov_b32 s24, s55
	s_and_b32 s29, s80, 0xffff
	s_mov_b32 s28, s79
	s_mov_b32 s16, s55
	s_mov_b32 s36, s79
	s_mov_b32 s38, s18
	s_mov_b32 s39, s19
	s_waitcnt lgkmcnt(2)
	v_mfma_f32_16x16x32_bf16 v[172:175], v[198:201], v[206:209], v[172:175]
	s_mov_b32 s17, s25
	s_mov_b32 s37, s29
	s_waitcnt vmcnt(5)
	v_mfma_f32_16x16x32_bf16 v[168:171], v[180:183], v[206:209], v[168:171]
	v_mfma_f32_16x16x32_bf16 v[164:167], v[202:205], v[206:209], v[164:167]
	v_mfma_f32_16x16x32_bf16 v[160:163], v[176:179], v[206:209], v[160:163]
	ds_read_b128 v[206:209], v186 offset:6144
	v_cvt_pk_bf16_f32 v15, v14, v15
	v_cvt_pk_bf16_f32 v14, v12, v13
	s_waitcnt lgkmcnt(2)
	v_mfma_f32_16x16x32_bf16 v[156:159], v[198:201], v[210:213], v[156:159]
	ds_write_b64 v185, v[14:15] offset:34816
	v_mfma_f32_16x16x32_bf16 v[152:155], v[180:183], v[210:213], v[152:155]
	v_mfma_f32_16x16x32_bf16 v[148:151], v[202:205], v[210:213], v[148:151]
	v_mfma_f32_16x16x32_bf16 v[144:147], v[176:179], v[210:213], v[144:147]
	buffer_load_dwordx4 v[12:15], v184, s[16:19], 0 offen
	ds_read_b128 v[210:213], v186 offset:8192
	s_waitcnt lgkmcnt(3)
	v_mfma_f32_16x16x32_bf16 v[132:135], v[198:201], v[214:217], v[132:135]
	v_mfma_f32_16x16x32_bf16 v[124:127], v[180:183], v[214:217], v[124:127]
	v_mfma_f32_16x16x32_bf16 v[120:123], v[202:205], v[214:217], v[120:123]
	v_mfma_f32_16x16x32_bf16 v[140:143], v[176:179], v[214:217], v[140:143]
	ds_read_b128 v[214:217], v186 offset:10240
	v_cvt_pk_bf16_f32 v3, v2, v3
	v_cvt_pk_bf16_f32 v2, v0, v1
	s_waitcnt lgkmcnt(3)
	v_mfma_f32_16x16x32_bf16 v[136:139], v[198:201], v[206:209], v[136:139]
	ds_write_b64 v185, v[2:3] offset:43520
	v_mfma_f32_16x16x32_bf16 v[128:131], v[180:183], v[206:209], v[128:131]
	v_mfma_f32_16x16x32_bf16 v[116:119], v[202:205], v[206:209], v[116:119]
	v_mfma_f32_16x16x32_bf16 v[112:115], v[176:179], v[206:209], v[112:115]
	buffer_load_dwordx4 v[0:3], v184, s[16:19], s19 offen
	ds_read_b128 v[206:209], v186 offset:12288
	s_waitcnt lgkmcnt(3)
	v_mfma_f32_16x16x32_bf16 v[100:103], v[198:201], v[210:213], v[100:103]
	v_mfma_f32_16x16x32_bf16 v[92:95], v[180:183], v[210:213], v[92:95]
	v_mfma_f32_16x16x32_bf16 v[88:91], v[202:205], v[210:213], v[88:91]
	v_mfma_f32_16x16x32_bf16 v[108:111], v[176:179], v[210:213], v[108:111]
	ds_read_b128 v[210:213], v186 offset:14336
	v_cvt_pk_bf16_f32 v31, v30, v31
	v_cvt_pk_bf16_f32 v30, v28, v29
	s_waitcnt lgkmcnt(3)
	v_mfma_f32_16x16x32_bf16 v[104:107], v[198:201], v[214:217], v[104:107]
	ds_write_b64 v185, v[30:31] offset:52224
	v_mfma_f32_16x16x32_bf16 v[96:99], v[180:183], v[214:217], v[96:99]
	v_mfma_f32_16x16x32_bf16 v[84:87], v[202:205], v[214:217], v[84:87]
	v_mfma_f32_16x16x32_bf16 v[80:83], v[176:179], v[214:217], v[80:83]
	buffer_load_dwordx4 v[28:31], v184, s[16:19], s87 offen
	ds_read_b128 v[214:217], v186 offset:16384
	s_waitcnt lgkmcnt(3)
	v_mfma_f32_16x16x32_bf16 v[72:75], v[198:201], v[206:209], v[72:75]
	v_mfma_f32_16x16x32_bf16 v[64:67], v[180:183], v[206:209], v[64:67]
	v_mfma_f32_16x16x32_bf16 v[60:63], v[202:205], v[206:209], v[60:63]
	v_mfma_f32_16x16x32_bf16 v[76:79], v[176:179], v[206:209], v[76:79]
	ds_read_b128 v[206:209], v186 offset:1024
	v_cvt_pk_bf16_f32 v27, v26, v27
	v_cvt_pk_bf16_f32 v26, v24, v25
	s_waitcnt lgkmcnt(3)
	v_mfma_f32_16x16x32_bf16 v[68:71], v[198:201], v[210:213], v[68:71]
	ds_write_b64 v185, v[26:27] offset:60928
	v_mfma_f32_16x16x32_bf16 v[56:59], v[180:183], v[210:213], v[56:59]
	v_mfma_f32_16x16x32_bf16 v[52:55], v[202:205], v[210:213], v[52:55]
	v_mfma_f32_16x16x32_bf16 v[48:51], v[176:179], v[210:213], v[48:51]
	buffer_load_dwordx4 v[24:27], v184, s[16:19], s88 offen
	ds_read_b128 v[210:213], v186 offset:3072
	s_waitcnt lgkmcnt(3)
	v_mfma_f32_16x16x32_bf16 v[44:47], v[198:201], v[214:217], v[44:47]
	ds_read_b64_tr_b16 v[200:201], v188 offset:17408
	ds_read_b64_tr_b16 v[220:221], v188 offset:17440
	ds_read_b64_tr_b16 v[198:199], v187 offset:17408
	ds_read_b64_tr_b16 v[218:219], v187 offset:17440
	v_mfma_f32_16x16x32_bf16 v[40:43], v[180:183], v[214:217], v[40:43]
	ds_read_b64_tr_b16 v[180:181], v187 offset:17472
	ds_read_b64_tr_b16 v[182:183], v188 offset:17472
	v_mfma_f32_16x16x32_bf16 v[32:35], v[176:179], v[214:217], v[32:35]
	ds_read_b64_tr_b16 v[176:177], v187 offset:17504
	ds_read_b64_tr_b16 v[178:179], v188 offset:17504
	v_mfma_f32_16x16x32_bf16 v[36:39], v[202:205], v[214:217], v[36:39]
	ds_read_b128 v[202:205], v186 offset:5120
	v_cvt_pk_bf16_f32 v23, v22, v23
	v_cvt_pk_bf16_f32 v22, v20, v21
	s_waitcnt lgkmcnt(6)
	v_mfma_f32_16x16x32_bf16 v[172:175], v[198:201], v[206:209], v[172:175]
	ds_write_b64 v185, v[22:23] offset:34880
	s_waitcnt lgkmcnt(6)
	v_mfma_f32_16x16x32_bf16 v[168:171], v[218:221], v[206:209], v[168:171]
	s_waitcnt lgkmcnt(4)
	v_mfma_f32_16x16x32_bf16 v[164:167], v[180:183], v[206:209], v[164:167]
	s_waitcnt lgkmcnt(2)
	v_mfma_f32_16x16x32_bf16 v[160:163], v[176:179], v[206:209], v[160:163]
	buffer_load_dwordx4 v[20:23], v184, s[36:39], 0 offen
	ds_read_b128 v[206:209], v186 offset:7168
	v_mfma_f32_16x16x32_bf16 v[156:159], v[198:201], v[210:213], v[156:159]
	v_mfma_f32_16x16x32_bf16 v[152:155], v[218:221], v[210:213], v[152:155]
	v_mfma_f32_16x16x32_bf16 v[148:151], v[180:183], v[210:213], v[148:151]
	v_mfma_f32_16x16x32_bf16 v[144:147], v[176:179], v[210:213], v[144:147]
	ds_read_b128 v[210:213], v186 offset:9216
	v_cvt_pk_bf16_f32 v7, v6, v7
	v_cvt_pk_bf16_f32 v6, v4, v5
	s_waitcnt lgkmcnt(3)
	v_mfma_f32_16x16x32_bf16 v[132:135], v[198:201], v[202:205], v[132:135]
	ds_write_b64 v185, v[6:7] offset:43584
	v_mfma_f32_16x16x32_bf16 v[124:127], v[218:221], v[202:205], v[124:127]
	v_mfma_f32_16x16x32_bf16 v[120:123], v[180:183], v[202:205], v[120:123]
	v_mfma_f32_16x16x32_bf16 v[140:143], v[176:179], v[202:205], v[140:143]
	buffer_load_dwordx4 v[4:7], v184, s[36:39], s19 offen
	ds_read_b128 v[202:205], v186 offset:11264
	s_waitcnt lgkmcnt(3)
	v_mfma_f32_16x16x32_bf16 v[136:139], v[198:201], v[206:209], v[136:139]
	v_mfma_f32_16x16x32_bf16 v[128:131], v[218:221], v[206:209], v[128:131]
	v_mfma_f32_16x16x32_bf16 v[116:119], v[180:183], v[206:209], v[116:119]
	v_mfma_f32_16x16x32_bf16 v[112:115], v[176:179], v[206:209], v[112:115]
	ds_read_b128 v[206:209], v186 offset:13312
	v_cvt_pk_bf16_f32 v11, v10, v11
	v_cvt_pk_bf16_f32 v10, v8, v9
	s_waitcnt lgkmcnt(3)
	v_mfma_f32_16x16x32_bf16 v[100:103], v[198:201], v[210:213], v[100:103]
	ds_write_b64 v185, v[10:11] offset:52288
	v_mfma_f32_16x16x32_bf16 v[92:95], v[218:221], v[210:213], v[92:95]
	v_mfma_f32_16x16x32_bf16 v[88:91], v[180:183], v[210:213], v[88:91]
	v_mfma_f32_16x16x32_bf16 v[108:111], v[176:179], v[210:213], v[108:111]
	buffer_load_dwordx4 v[8:11], v184, s[36:39], s87 offen
	ds_read_b128 v[210:213], v186 offset:15360
	s_waitcnt lgkmcnt(3)
	v_mfma_f32_16x16x32_bf16 v[104:107], v[198:201], v[202:205], v[104:107]
	v_mfma_f32_16x16x32_bf16 v[96:99], v[218:221], v[202:205], v[96:99]
	v_mfma_f32_16x16x32_bf16 v[84:87], v[180:183], v[202:205], v[84:87]
	v_mfma_f32_16x16x32_bf16 v[80:83], v[176:179], v[202:205], v[80:83]
	ds_read_b128 v[202:205], v186 offset:17408
	v_cvt_pk_bf16_f32 v19, v18, v19
	v_cvt_pk_bf16_f32 v18, v16, v17
	s_waitcnt lgkmcnt(3)
	v_mfma_f32_16x16x32_bf16 v[72:75], v[198:201], v[206:209], v[72:75]
	ds_write_b64 v185, v[18:19] offset:60992
	v_mfma_f32_16x16x32_bf16 v[64:67], v[218:221], v[206:209], v[64:67]
	v_mfma_f32_16x16x32_bf16 v[60:63], v[180:183], v[206:209], v[60:63]
	v_mfma_f32_16x16x32_bf16 v[76:79], v[176:179], v[206:209], v[76:79]
	buffer_load_dwordx4 v[16:19], v184, s[36:39], s88 offen
	s_waitcnt lgkmcnt(2)
	v_mfma_f32_16x16x32_bf16 v[68:71], v[198:201], v[210:213], v[68:71]
	v_mfma_f32_16x16x32_bf16 v[56:59], v[218:221], v[210:213], v[56:59]
	v_mfma_f32_16x16x32_bf16 v[52:55], v[180:183], v[210:213], v[52:55]
	v_mfma_f32_16x16x32_bf16 v[48:51], v[176:179], v[210:213], v[48:51]
	s_waitcnt lgkmcnt(1)
	v_mfma_f32_16x16x32_bf16 v[44:47], v[198:201], v[202:205], v[44:47]
	v_mfma_f32_16x16x32_bf16 v[40:43], v[218:221], v[202:205], v[40:43]
	v_mfma_f32_16x16x32_bf16 v[36:39], v[180:183], v[202:205], v[36:39]
	v_mfma_f32_16x16x32_bf16 v[32:35], v[176:179], v[202:205], v[32:35]
	s_waitcnt vmcnt(8)
	v_lshlrev_b32_e32 v189, 10, v192
	v_lshlrev_b32_e32 v192, 10, v193
	v_lshlrev_b32_e32 v193, 10, v195
	v_lshlrev_b32_e32 v195, 10, v191
	v_lshlrev_b32_e32 v243, 10, v190
	v_and_or_b32 v189, v189, s83, v197
	v_and_or_b32 v192, v192, s83, v197
	v_and_or_b32 v191, v193, s83, v197
	v_and_or_b32 v190, v195, s83, v197
	v_and_or_b32 v193, v243, s83, v197
	s_mov_b32 m0, s46
	s_waitcnt lgkmcnt(0)
	s_barrier
	v_mbcnt_lo_u32_b32 v244, -1, 0
	v_mbcnt_hi_u32_b32 v244, -1, v244
	s_add_i32 s100, s54, s4
	v_ashrrev_i32_e32 v238, 1, v244
	v_and_b32_e32 v238, -8, v238
	v_add_u32_e32 v244, s100, v238
	v_ashrrev_i32_e32 v245, 31, v244
	v_lshlrev_b64 v[238:239], 2, v[244:245]
	v_lshl_add_u64 v[240:241], s[56:57], 0, v[238:239]
	v_lshl_add_u64 v[238:239], s[58:59], 0, v[238:239]
	global_load_dwordx4 v[252:255], v[240:241], off
	global_load_dwordx4 v[248:251], v[238:239], off
	global_load_dwordx4 v[244:247], v[240:241], off offset:16
	s_nop 0
	global_load_dwordx4 v[238:241], v[238:239], off offset:16
	ds_read_b64_tr_b16 v[178:179], v188 offset:34816
	ds_read_b64_tr_b16 v[176:177], v187 offset:34816
	ds_read_b64_tr_b16 v[180:181], v187 offset:34848
	ds_read_b64_tr_b16 v[198:199], v187 offset:34880
	ds_read_b64_tr_b16 v[202:203], v187 offset:34912
	ds_read_b128 v[206:209], v186 offset:36864
	ds_read_b64_tr_b16 v[182:183], v188 offset:34848
	ds_read_b64_tr_b16 v[200:201], v188 offset:34880
	ds_read_b64_tr_b16 v[204:205], v188 offset:34912
	ds_read_b128 v[210:213], v186 offset:38912
	ds_read_b128 v[214:217], v186 offset:40960
	buffer_load_dwordx4 v189, s[20:23], 0 offen lds
	s_mov_b32 m0, s86
	s_waitcnt lgkmcnt(5)
	v_mfma_f32_16x16x32_bf16 v[172:175], v[176:179], v[206:209], v[172:175]
	buffer_load_dwordx4 v192, s[20:23], 0 offen lds
	s_mov_b32 m0, s89
	s_nop 0
	buffer_load_dwordx4 v191, s[20:23], 0 offen lds
	s_mov_b32 m0, s90
	s_waitcnt lgkmcnt(4)
	v_mfma_f32_16x16x32_bf16 v[168:171], v[180:183], v[206:209], v[168:171]
	buffer_load_dwordx4 v190, s[20:23], 0 offen lds
	s_mov_b32 m0, s91
	s_nop 0
	buffer_load_dwordx4 v193, s[20:23], 0 offen lds
	s_waitcnt lgkmcnt(3)
	v_mfma_f32_16x16x32_bf16 v[164:167], v[198:201], v[206:209], v[164:167]
	s_waitcnt lgkmcnt(2)
	v_mfma_f32_16x16x32_bf16 v[160:163], v[202:205], v[206:209], v[160:163]
	ds_read_b128 v[206:209], v186 offset:43008
	s_waitcnt vmcnt(16)
	v_cvt_pk_bf16_f32 v15, v14, v15
	v_cvt_pk_bf16_f32 v14, v12, v13
	s_waitcnt lgkmcnt(2)
	v_mfma_f32_16x16x32_bf16 v[156:159], v[176:179], v[210:213], v[156:159]
	ds_write_b64 v185, v[14:15]
	v_mfma_f32_16x16x32_bf16 v[152:155], v[180:183], v[210:213], v[152:155]
	v_mfma_f32_16x16x32_bf16 v[148:151], v[198:201], v[210:213], v[148:151]
	v_mfma_f32_16x16x32_bf16 v[144:147], v[202:205], v[210:213], v[144:147]
	buffer_load_dwordx4 v[12:15], v184, s[16:19], s93 offen
	ds_read_b128 v[210:213], v186 offset:45056
	s_waitcnt lgkmcnt(3)
	v_mfma_f32_16x16x32_bf16 v[132:135], v[176:179], v[214:217], v[132:135]
	v_mfma_f32_16x16x32_bf16 v[124:127], v[180:183], v[214:217], v[124:127]
	v_mfma_f32_16x16x32_bf16 v[120:123], v[198:201], v[214:217], v[120:123]
	v_mfma_f32_16x16x32_bf16 v[140:143], v[202:205], v[214:217], v[140:143]
	ds_read_b128 v[214:217], v186 offset:47104
	s_waitcnt vmcnt(16)
	v_cvt_pk_bf16_f32 v3, v2, v3
	v_cvt_pk_bf16_f32 v2, v0, v1
	s_waitcnt lgkmcnt(3)
	v_mfma_f32_16x16x32_bf16 v[136:139], v[176:179], v[206:209], v[136:139]
	ds_write_b64 v185, v[2:3] offset:8704
	v_mfma_f32_16x16x32_bf16 v[128:131], v[180:183], v[206:209], v[128:131]
	v_mfma_f32_16x16x32_bf16 v[116:119], v[198:201], v[206:209], v[116:119]
	v_mfma_f32_16x16x32_bf16 v[112:115], v[202:205], v[206:209], v[112:115]
	buffer_load_dwordx4 v[0:3], v184, s[16:19], s94 offen
	ds_read_b128 v[206:209], v186 offset:49152
	s_waitcnt lgkmcnt(3)
	v_mfma_f32_16x16x32_bf16 v[100:103], v[176:179], v[210:213], v[100:103]
	v_mfma_f32_16x16x32_bf16 v[92:95], v[180:183], v[210:213], v[92:95]
	v_mfma_f32_16x16x32_bf16 v[88:91], v[198:201], v[210:213], v[88:91]
	v_mfma_f32_16x16x32_bf16 v[108:111], v[202:205], v[210:213], v[108:111]
	ds_read_b128 v[210:213], v186 offset:51200
	s_waitcnt vmcnt(16)
	v_cvt_pk_bf16_f32 v31, v30, v31
	v_cvt_pk_bf16_f32 v30, v28, v29
	s_waitcnt lgkmcnt(3)
	v_mfma_f32_16x16x32_bf16 v[104:107], v[176:179], v[214:217], v[104:107]
	ds_write_b64 v185, v[30:31] offset:17408
	v_mfma_f32_16x16x32_bf16 v[96:99], v[180:183], v[214:217], v[96:99]
	v_mfma_f32_16x16x32_bf16 v[84:87], v[198:201], v[214:217], v[84:87]
	v_mfma_f32_16x16x32_bf16 v[80:83], v[202:205], v[214:217], v[80:83]
	buffer_load_dwordx4 v[28:31], v184, s[16:19], s95 offen
	ds_read_b128 v[214:217], v186 offset:53248
	s_waitcnt lgkmcnt(3)
	v_mfma_f32_16x16x32_bf16 v[72:75], v[176:179], v[206:209], v[72:75]
	v_mfma_f32_16x16x32_bf16 v[64:67], v[180:183], v[206:209], v[64:67]
	v_mfma_f32_16x16x32_bf16 v[60:63], v[198:201], v[206:209], v[60:63]
	v_mfma_f32_16x16x32_bf16 v[76:79], v[202:205], v[206:209], v[76:79]
	ds_read_b128 v[206:209], v186 offset:37888
	s_waitcnt vmcnt(16)
	v_cvt_pk_bf16_f32 v27, v26, v27
	v_cvt_pk_bf16_f32 v26, v24, v25
	s_waitcnt lgkmcnt(3)
	v_mfma_f32_16x16x32_bf16 v[68:71], v[176:179], v[210:213], v[68:71]
	ds_write_b64 v185, v[26:27] offset:26112
	v_mfma_f32_16x16x32_bf16 v[56:59], v[180:183], v[210:213], v[56:59]
	v_mfma_f32_16x16x32_bf16 v[52:55], v[198:201], v[210:213], v[52:55]
	v_mfma_f32_16x16x32_bf16 v[48:51], v[202:205], v[210:213], v[48:51]
	buffer_load_dwordx4 v[24:27], v184, s[16:19], s96 offen
	ds_read_b128 v[210:213], v186 offset:39936
	s_waitcnt lgkmcnt(3)
	v_mfma_f32_16x16x32_bf16 v[44:47], v[176:179], v[214:217], v[44:47]
	ds_read_b64_tr_b16 v[178:179], v188 offset:52224
	ds_read_b64_tr_b16 v[220:221], v188 offset:52256
	ds_read_b64_tr_b16 v[176:177], v187 offset:52224
	ds_read_b64_tr_b16 v[218:219], v187 offset:52256
	v_mfma_f32_16x16x32_bf16 v[40:43], v[180:183], v[214:217], v[40:43]
	v_mfma_f32_16x16x32_bf16 v[180:183], v[198:201], v[214:217], v[36:39]
	ds_read_b64_tr_b16 v[198:199], v187 offset:52288
	ds_read_b64_tr_b16 v[200:201], v188 offset:52288
	v_mfma_f32_16x16x32_bf16 v[32:35], v[202:205], v[214:217], v[32:35]
	ds_read_b64_tr_b16 v[202:203], v187 offset:52320
	ds_read_b64_tr_b16 v[204:205], v188 offset:52320
	ds_read_b128 v[36:39], v186 offset:41984
	s_waitcnt vmcnt(16)
	v_cvt_pk_bf16_f32 v23, v22, v23
	v_cvt_pk_bf16_f32 v22, v20, v21
	s_waitcnt lgkmcnt(6)
	v_mfma_f32_16x16x32_bf16 v[214:217], v[176:179], v[206:209], v[172:175]
	ds_write_b64 v185, v[22:23] offset:64
	s_waitcnt lgkmcnt(6)
	v_mfma_f32_16x16x32_bf16 v[222:225], v[218:221], v[206:209], v[168:171]
	s_waitcnt lgkmcnt(4)
	v_mfma_f32_16x16x32_bf16 v[226:229], v[198:201], v[206:209], v[164:167]
	s_waitcnt lgkmcnt(2)
	v_mfma_f32_16x16x32_bf16 v[206:209], v[202:205], v[206:209], v[160:163]
	buffer_load_dwordx4 v[20:23], v184, s[36:39], s93 offen
	ds_read_b128 v[230:233], v186 offset:44032
	v_mfma_f32_16x16x32_bf16 v[172:175], v[176:179], v[210:213], v[156:159]
	v_mfma_f32_16x16x32_bf16 v[164:167], v[218:221], v[210:213], v[152:155]
	v_mfma_f32_16x16x32_bf16 v[168:171], v[198:201], v[210:213], v[148:151]
	v_mfma_f32_16x16x32_bf16 v[160:163], v[202:205], v[210:213], v[144:147]
	ds_read_b128 v[210:213], v186 offset:46080
	s_waitcnt vmcnt(16)
	v_cvt_pk_bf16_f32 v7, v6, v7
	v_cvt_pk_bf16_f32 v6, v4, v5
	s_waitcnt lgkmcnt(3)
	v_mfma_f32_16x16x32_bf16 v[156:159], v[176:179], v[36:39], v[132:135]
	ds_write_b64 v185, v[6:7] offset:8768
	v_mfma_f32_16x16x32_bf16 v[144:147], v[218:221], v[36:39], v[124:127]
	v_mfma_f32_16x16x32_bf16 v[152:155], v[198:201], v[36:39], v[120:123]
	v_mfma_f32_16x16x32_bf16 v[148:151], v[202:205], v[36:39], v[140:143]
	buffer_load_dwordx4 v[4:7], v184, s[36:39], s94 offen
	ds_read_b128 v[36:39], v186 offset:48128
	s_waitcnt lgkmcnt(3)
	v_mfma_f32_16x16x32_bf16 v[140:143], v[176:179], v[230:233], v[136:139]
	v_mfma_f32_16x16x32_bf16 v[132:135], v[218:221], v[230:233], v[128:131]
	v_mfma_f32_16x16x32_bf16 v[136:139], v[198:201], v[230:233], v[116:119]
	v_mfma_f32_16x16x32_bf16 v[128:131], v[202:205], v[230:233], v[112:115]
	ds_read_b128 v[230:233], v186 offset:50176
	s_waitcnt vmcnt(16)
	v_cvt_pk_bf16_f32 v11, v10, v11
	v_cvt_pk_bf16_f32 v10, v8, v9
	s_waitcnt lgkmcnt(3)
	v_mfma_f32_16x16x32_bf16 v[124:127], v[176:179], v[210:213], v[100:103]
	ds_write_b64 v185, v[10:11] offset:17472
	v_mfma_f32_16x16x32_bf16 v[112:115], v[218:221], v[210:213], v[92:95]
	v_mfma_f32_16x16x32_bf16 v[120:123], v[198:201], v[210:213], v[88:91]
	v_mfma_f32_16x16x32_bf16 v[116:119], v[202:205], v[210:213], v[108:111]
	buffer_load_dwordx4 v[8:11], v184, s[36:39], s95 offen
	ds_read_b128 v[210:213], v186 offset:52224
	s_waitcnt lgkmcnt(3)
	v_mfma_f32_16x16x32_bf16 v[108:111], v[176:179], v[36:39], v[104:107]
	v_mfma_f32_16x16x32_bf16 v[100:103], v[218:221], v[36:39], v[96:99]
	v_mfma_f32_16x16x32_bf16 v[104:107], v[198:201], v[36:39], v[84:87]
	v_mfma_f32_16x16x32_bf16 v[96:99], v[202:205], v[36:39], v[80:83]
	ds_read_b128 v[234:237], v186 offset:54272
	s_waitcnt vmcnt(16)
	v_cvt_pk_bf16_f32 v19, v18, v19
	v_cvt_pk_bf16_f32 v18, v16, v17
	s_waitcnt lgkmcnt(3)
	v_mfma_f32_16x16x32_bf16 v[92:95], v[176:179], v[230:233], v[72:75]
	ds_write_b64 v185, v[18:19] offset:26176
	v_mfma_f32_16x16x32_bf16 v[80:83], v[218:221], v[230:233], v[64:67]
	v_mfma_f32_16x16x32_bf16 v[88:91], v[198:201], v[230:233], v[60:63]
	v_mfma_f32_16x16x32_bf16 v[84:87], v[202:205], v[230:233], v[76:79]
	buffer_load_dwordx4 v[16:19], v184, s[36:39], s96 offen
	s_waitcnt lgkmcnt(2)
	v_mfma_f32_16x16x32_bf16 v[76:79], v[176:179], v[210:213], v[68:71]
	v_mfma_f32_16x16x32_bf16 v[68:71], v[218:221], v[210:213], v[56:59]
	v_mfma_f32_16x16x32_bf16 v[72:75], v[198:201], v[210:213], v[52:55]
	v_mfma_f32_16x16x32_bf16 v[64:67], v[202:205], v[210:213], v[48:51]
	s_waitcnt lgkmcnt(1)
	v_mfma_f32_16x16x32_bf16 v[52:55], v[176:179], v[234:237], v[44:47]
	v_mfma_f32_16x16x32_bf16 v[36:39], v[218:221], v[234:237], v[40:43]
	v_mfma_f32_16x16x32_bf16 v[48:51], v[198:201], v[234:237], v[180:183]
	v_mfma_f32_16x16x32_bf16 v[32:35], v[202:205], v[234:237], v[32:35]
	s_waitcnt vmcnt(8)
	s_waitcnt lgkmcnt(0)
	s_barrier
	v_mbcnt_lo_u32_b32 v178, -1, 0
	v_mbcnt_hi_u32_b32 v178, -1, v178
	s_add_i32 s16, s54, s4
	v_ashrrev_i32_e32 v40, 1, v178
	v_and_b32_e32 v40, -8, v40
	v_add_u32_e32 v176, s16, v40
	v_ashrrev_i32_e32 v177, 31, v176
	v_lshlrev_b64 v[40:41], 2, v[176:177]
	v_lshl_add_u64 v[42:43], s[56:57], 0, v[40:41]
	v_lshl_add_u64 v[40:41], s[58:59], 0, v[40:41]
	s_nop 0
	s_mul_i32 s16, s72, 0x90
	v_and_or_b32 v178, v178, 15, s16
	v_add_u32_e32 v180, s68, v178
	v_ashrrev_i32_e32 v181, 31, v180
	v_lshlrev_b64 v[180:181], 12, v[180:181]
	v_lshl_add_u64 v[198:199], s[50:51], 0, v[180:181]
	v_lshlrev_b64 v[176:177], 1, v[176:177]
	v_lshl_add_u64 v[198:199], v[198:199], 0, v[176:177]
	s_add_i32 s16, s68, 0x50
	s_and_b64 vcc, exec, s[30:31]
	s_mov_b32 s54, s42
	s_mov_b64 s[58:59], s[62:63]
	s_mov_b64 s[56:57], s[60:61]
	s_mov_b64 s[30:31], s[18:19]
	s_mov_b64 s[26:27], s[18:19]
	v_add_f32_e32 v179, v214, v252
	v_add_f32_e32 v181, v226, v248
	v_add_f32_e32 v183, v215, v253
	v_add_f32_e32 v197, v216, v254
	v_add_f32_e32 v201, v228, v250
	v_add_f32_e32 v203, v217, v255
	v_add_f32_e32 v195, v227, v249
	v_add_f32_e32 v204, v229, v251
	v_add_f32_e32 v205, v222, v244
	v_add_f32_e32 v210, v223, v245
	v_add_f32_e32 v211, v224, v246
	s_waitcnt vmcnt(0)
	v_add_f32_e32 v212, v208, v240
	v_add_f32_e32 v213, v225, v247
	v_min_f32_e32 v180, 0x40e00000, v179
	v_med3_f32 v182, v181, s53, v194
	v_min_f32_e32 v181, 0x40e00000, v183
	v_min_f32_e32 v200, 0x40e00000, v197
	v_med3_f32 v202, v201, s53, v194
	v_min_f32_e32 v201, 0x40e00000, v203
	v_add_f32_e32 v214, v209, v241
	v_med3_f32 v183, v195, s53, v194
	v_med3_f32 v203, v204, s53, v194
	v_min_f32_e32 v204, 0x40e00000, v205
	v_min_f32_e32 v205, 0x40e00000, v210
	v_min_f32_e32 v208, 0x40e00000, v211
	v_med3_f32 v210, v212, s53, v194
	v_min_f32_e32 v209, 0x40e00000, v213
	v_mul_f32_e32 v179, 0x3fd9db23, v180
	v_mul_f32_e32 v195, 0x3fd9db23, v181
	v_mul_f32_e32 v197, 0x3fd9db23, v200
	v_mul_f32_e32 v212, 0x3fd9db23, v201
	v_med3_f32 v211, v214, s53, v194
	v_pk_add_f32 v[182:183], v[182:183], 1.0 op_sel_hi:[1,0]
	v_pk_add_f32 v[202:203], v[202:203], 1.0 op_sel_hi:[1,0]
	v_mul_f32_e32 v213, 0x3fd9db23, v204
	v_mul_f32_e32 v214, 0x3fd9db23, v205
	v_mul_f32_e32 v215, 0x3fd9db23, v208
	v_mul_f32_e32 v216, 0x3fd9db23, v209
	v_mul_f32_e32 v179, 0xbfb8aa3b, v179
	v_mul_f32_e32 v195, 0xbfb8aa3b, v195
	v_mul_f32_e32 v197, 0xbfb8aa3b, v197
	v_mul_f32_e32 v212, 0xbfb8aa3b, v212
	v_pk_mul_f32 v[200:201], v[200:201], v[202:203]
	v_pk_mul_f32 v[180:181], v[180:181], v[182:183]
	v_mul_f32_e32 v182, 0xbfb8aa3b, v213
	v_mul_f32_e32 v183, 0xbfb8aa3b, v214
	v_mul_f32_e32 v202, 0xbfb8aa3b, v215
	v_mul_f32_e32 v203, 0xbfb8aa3b, v216
	v_exp_f32_e32 v179, v179
	v_exp_f32_e32 v195, v195
	v_exp_f32_e32 v197, v197
	v_exp_f32_e32 v212, v212
	v_exp_f32_e32 v182, v182
	v_exp_f32_e32 v183, v183
	v_exp_f32_e32 v202, v202
	v_exp_f32_e32 v203, v203
	v_add_f32_e32 v179, 1.0, v179
	v_add_f32_e32 v195, 1.0, v195
	v_add_f32_e32 v197, 1.0, v197
	v_add_f32_e32 v212, 1.0, v212
	v_add_f32_e32 v213, 1.0, v182
	v_add_f32_e32 v214, 1.0, v183
	v_add_f32_e32 v215, 1.0, v202
	v_add_f32_e32 v216, 1.0, v203
	v_rcp_f32_e32 v182, v179
	v_rcp_f32_e32 v183, v195
	v_rcp_f32_e32 v202, v197
	v_rcp_f32_e32 v203, v212
	v_add_f32_e32 v206, v206, v238
	v_add_f32_e32 v207, v207, v239
	v_rcp_f32_e32 v212, v213
	v_rcp_f32_e32 v213, v214
	v_rcp_f32_e32 v214, v215
	v_rcp_f32_e32 v215, v216
	v_med3_f32 v206, v206, s53, v194
	v_med3_f32 v207, v207, s53, v194
	v_pk_mul_f32 v[182:183], v[180:181], v[182:183]
	v_pk_mul_f32 v[180:181], v[200:201], v[202:203]
	v_pk_add_f32 v[206:207], v[206:207], 1.0 op_sel_hi:[1,0]
	v_cvt_pk_bf16_f32 v181, v180, v181
	v_cvt_pk_bf16_f32 v180, v182, v183
	v_pk_add_f32 v[182:183], v[210:211], 1.0 op_sel_hi:[1,0]
	v_pk_mul_f32 v[200:201], v[204:205], v[206:207]
	v_pk_mul_f32 v[182:183], v[208:209], v[182:183]
	v_add_f32_e32 v172, v172, v252
	v_pk_mul_f32 v[200:201], v[200:201], v[212:213]
	v_pk_mul_f32 v[182:183], v[182:183], v[214:215]
	v_min_f32_e32 v172, 0x40e00000, v172
	v_add_f32_e32 v173, v173, v253
	v_cvt_pk_bf16_f32 v183, v182, v183
	v_cvt_pk_bf16_f32 v182, v200, v201
	v_mul_f32_e32 v179, 0x3fd9db23, v172
	v_min_f32_e32 v173, 0x40e00000, v173
	global_store_dwordx4 v[198:199], v[180:183], off
	v_mul_f32_e32 v179, 0xbfb8aa3b, v179
	v_exp_f32_e32 v179, v179
	v_mul_f32_e32 v182, 0x3fd9db23, v173
	v_mul_f32_e32 v182, 0xbfb8aa3b, v182
	v_exp_f32_e32 v183, v182
	v_add_f32_e32 v174, v174, v254
	v_add_f32_e32 v179, 1.0, v179
	v_min_f32_e32 v174, 0x40e00000, v174
	v_rcp_f32_e32 v182, v179
	v_add_f32_e32 v179, 1.0, v183
	v_mul_f32_e32 v183, 0x3fd9db23, v174
	v_mul_f32_e32 v183, 0xbfb8aa3b, v183
	v_exp_f32_e32 v195, v183
	v_add_f32_e32 v175, v175, v255
	v_min_f32_e32 v175, 0x40e00000, v175
	v_rcp_f32_e32 v183, v179
	v_add_f32_e32 v179, 1.0, v195
	v_mul_f32_e32 v195, 0x3fd9db23, v175
	v_mul_f32_e32 v195, 0xbfb8aa3b, v195
	v_exp_f32_e32 v195, v195
	v_rcp_f32_e32 v198, v179
	v_add_f32_e32 v168, v168, v248
	v_add_f32_e32 v169, v169, v249
	v_add_f32_e32 v179, 1.0, v195
	v_add_f32_e32 v170, v170, v250
	v_add_f32_e32 v171, v171, v251
	v_rcp_f32_e32 v199, v179
	v_med3_f32 v168, v168, s53, v194
	v_med3_f32 v169, v169, s53, v194
	v_med3_f32 v170, v170, s53, v194
	v_med3_f32 v171, v171, s53, v194
	v_pk_add_f32 v[168:169], v[168:169], 1.0 op_sel_hi:[1,0]
	v_pk_add_f32 v[170:171], v[170:171], 1.0 op_sel_hi:[1,0]
	v_pk_mul_f32 v[168:169], v[172:173], v[168:169]
	v_pk_mul_f32 v[170:171], v[174:175], v[170:171]
	v_add_f32_e32 v164, v164, v244
	v_pk_mul_f32 v[172:173], v[168:169], v[182:183]
	v_pk_mul_f32 v[168:169], v[170:171], v[198:199]
	v_min_f32_e32 v164, 0x40e00000, v164
	v_cvt_pk_bf16_f32 v169, v168, v169
	v_mul_f32_e32 v168, 0x3fd9db23, v164
	v_add_f32_e32 v166, v166, v246
	v_add_f32_e32 v167, v167, v247
	v_mul_f32_e32 v168, 0xbfb8aa3b, v168
	v_add_f32_e32 v165, v165, v245
	v_min_f32_e32 v166, 0x40e00000, v166
	v_min_f32_e32 v167, 0x40e00000, v167
	v_exp_f32_e32 v170, v168
	v_cvt_pk_bf16_f32 v168, v172, v173
	v_min_f32_e32 v165, 0x40e00000, v165
	v_mul_f32_e32 v172, 0x3fd9db23, v166
	v_mul_f32_e32 v173, 0x3fd9db23, v167
	v_mul_f32_e32 v171, 0x3fd9db23, v165
	v_mul_f32_e32 v172, 0xbfb8aa3b, v172
	v_mul_f32_e32 v173, 0xbfb8aa3b, v173
	v_mul_f32_e32 v171, 0xbfb8aa3b, v171
	v_exp_f32_e32 v172, v172
	v_exp_f32_e32 v173, v173
	v_exp_f32_e32 v171, v171
	v_add_f32_e32 v170, 1.0, v170
	v_add_f32_e32 v172, 1.0, v172
	v_add_f32_e32 v173, 1.0, v173
	v_add_f32_e32 v171, 1.0, v171
	v_add_f32_e32 v162, v162, v240
	v_rcp_f32_e32 v172, v172
	v_add_f32_e32 v163, v163, v241
	v_rcp_f32_e32 v173, v173
	v_add_f32_e32 v160, v160, v238
	v_rcp_f32_e32 v170, v170
	v_add_f32_e32 v161, v161, v239
	v_rcp_f32_e32 v171, v171
	v_med3_f32 v162, v162, s53, v194
	v_med3_f32 v163, v163, s53, v194
	v_med3_f32 v160, v160, s53, v194
	v_med3_f32 v161, v161, s53, v194
	v_pk_add_f32 v[162:163], v[162:163], 1.0 op_sel_hi:[1,0]
	v_pk_add_f32 v[160:161], v[160:161], 1.0 op_sel_hi:[1,0]
	v_pk_mul_f32 v[162:163], v[166:167], v[162:163]
	v_add_f32_e32 v156, v156, v252
	v_add_f32_e32 v157, v157, v253
	v_add_f32_e32 v158, v158, v254
	v_add_f32_e32 v159, v159, v255
	v_pk_mul_f32 v[160:161], v[164:165], v[160:161]
	v_pk_mul_f32 v[162:163], v[162:163], v[172:173]
	v_min_f32_e32 v156, 0x40e00000, v156
	v_min_f32_e32 v157, 0x40e00000, v157
	v_min_f32_e32 v158, 0x40e00000, v158
	v_min_f32_e32 v159, 0x40e00000, v159
	v_pk_mul_f32 v[160:161], v[160:161], v[170:171]
	v_cvt_pk_bf16_f32 v171, v162, v163
	v_mul_f32_e32 v162, 0x3fd9db23, v156
	v_mul_f32_e32 v163, 0x3fd9db23, v157
	v_mul_f32_e32 v164, 0x3fd9db23, v158
	v_mul_f32_e32 v165, 0x3fd9db23, v159
	v_mul_f32_e32 v162, 0xbfb8aa3b, v162
	v_mul_f32_e32 v163, 0xbfb8aa3b, v163
	v_mul_f32_e32 v164, 0xbfb8aa3b, v164
	v_mul_f32_e32 v165, 0xbfb8aa3b, v165
	v_exp_f32_e32 v162, v162
	v_exp_f32_e32 v163, v163
	v_exp_f32_e32 v164, v164
	v_exp_f32_e32 v165, v165
	v_add_f32_e32 v162, 1.0, v162
	v_add_f32_e32 v163, 1.0, v163
	v_add_f32_e32 v164, 1.0, v164
	v_add_f32_e32 v165, 1.0, v165
	v_add_f32_e32 v152, v152, v248
	v_rcp_f32_e32 v162, v162
	v_add_f32_e32 v153, v153, v249
	v_rcp_f32_e32 v163, v163
	v_add_f32_e32 v154, v154, v250
	v_rcp_f32_e32 v164, v164
	v_add_f32_e32 v155, v155, v251
	v_rcp_f32_e32 v165, v165
	v_med3_f32 v152, v152, s53, v194
	v_med3_f32 v153, v153, s53, v194
	v_med3_f32 v154, v154, s53, v194
	v_med3_f32 v155, v155, s53, v194
	v_pk_add_f32 v[152:153], v[152:153], 1.0 op_sel_hi:[1,0]
	v_pk_add_f32 v[154:155], v[154:155], 1.0 op_sel_hi:[1,0]
	v_pk_mul_f32 v[152:153], v[156:157], v[152:153]
	v_pk_mul_f32 v[154:155], v[158:159], v[154:155]
	v_add_f32_e32 v144, v144, v244
	v_pk_mul_f32 v[156:157], v[152:153], v[162:163]
	v_pk_mul_f32 v[152:153], v[154:155], v[164:165]
	v_min_f32_e32 v144, 0x40e00000, v144
	v_cvt_pk_bf16_f32 v153, v152, v153
	v_mul_f32_e32 v152, 0x3fd9db23, v144
	v_add_f32_e32 v146, v146, v246
	v_add_f32_e32 v147, v147, v247
	v_mul_f32_e32 v152, 0xbfb8aa3b, v152
	v_add_f32_e32 v145, v145, v245
	v_min_f32_e32 v146, 0x40e00000, v146
	v_min_f32_e32 v147, 0x40e00000, v147
	v_exp_f32_e32 v154, v152
	v_cvt_pk_bf16_f32 v152, v156, v157
	v_min_f32_e32 v145, 0x40e00000, v145
	v_mul_f32_e32 v156, 0x3fd9db23, v146
	v_mul_f32_e32 v157, 0x3fd9db23, v147
	v_mul_f32_e32 v155, 0x3fd9db23, v145
	v_mul_f32_e32 v156, 0xbfb8aa3b, v156
	v_mul_f32_e32 v157, 0xbfb8aa3b, v157
	v_mul_f32_e32 v155, 0xbfb8aa3b, v155
	v_exp_f32_e32 v156, v156
	v_exp_f32_e32 v157, v157
	v_exp_f32_e32 v155, v155
	v_add_f32_e32 v154, 1.0, v154
	v_add_f32_e32 v156, 1.0, v156
	v_add_f32_e32 v157, 1.0, v157
	v_add_f32_e32 v155, 1.0, v155
	v_add_f32_e32 v150, v150, v240
	v_rcp_f32_e32 v156, v156
	v_add_f32_e32 v151, v151, v241
	v_rcp_f32_e32 v157, v157
	v_add_f32_e32 v148, v148, v238
	v_rcp_f32_e32 v154, v154
	v_add_f32_e32 v149, v149, v239
	v_rcp_f32_e32 v155, v155
	v_med3_f32 v150, v150, s53, v194
	v_med3_f32 v151, v151, s53, v194
	v_med3_f32 v148, v148, s53, v194
	v_med3_f32 v149, v149, s53, v194
	v_pk_add_f32 v[150:151], v[150:151], 1.0 op_sel_hi:[1,0]
	v_pk_add_f32 v[148:149], v[148:149], 1.0 op_sel_hi:[1,0]
	v_pk_mul_f32 v[146:147], v[146:147], v[150:151]
	v_add_f32_e32 v140, v140, v252
	v_add_f32_e32 v141, v141, v253
	v_add_f32_e32 v142, v142, v254
	v_add_f32_e32 v143, v143, v255
	v_pk_mul_f32 v[144:145], v[144:145], v[148:149]
	v_pk_mul_f32 v[146:147], v[146:147], v[156:157]
	v_min_f32_e32 v140, 0x40e00000, v140
	v_min_f32_e32 v141, 0x40e00000, v141
	v_min_f32_e32 v142, 0x40e00000, v142
	v_min_f32_e32 v143, 0x40e00000, v143
	v_pk_mul_f32 v[144:145], v[144:145], v[154:155]
	v_cvt_pk_bf16_f32 v155, v146, v147
	v_mul_f32_e32 v146, 0x3fd9db23, v140
	v_mul_f32_e32 v147, 0x3fd9db23, v141
	v_mul_f32_e32 v148, 0x3fd9db23, v142
	v_mul_f32_e32 v149, 0x3fd9db23, v143
	v_mul_f32_e32 v146, 0xbfb8aa3b, v146
	v_mul_f32_e32 v147, 0xbfb8aa3b, v147
	v_mul_f32_e32 v148, 0xbfb8aa3b, v148
	v_mul_f32_e32 v149, 0xbfb8aa3b, v149
	v_exp_f32_e32 v146, v146
	v_exp_f32_e32 v147, v147
	v_exp_f32_e32 v148, v148
	v_exp_f32_e32 v149, v149
	v_add_f32_e32 v146, 1.0, v146
	v_add_f32_e32 v147, 1.0, v147
	v_add_f32_e32 v148, 1.0, v148
	v_add_f32_e32 v149, 1.0, v149
	v_add_f32_e32 v136, v136, v248
	v_rcp_f32_e32 v146, v146
	v_add_f32_e32 v137, v137, v249
	v_rcp_f32_e32 v147, v147
	v_add_f32_e32 v138, v138, v250
	v_rcp_f32_e32 v148, v148
	v_add_f32_e32 v139, v139, v251
	v_rcp_f32_e32 v149, v149
	v_med3_f32 v136, v136, s53, v194
	v_med3_f32 v137, v137, s53, v194
	v_med3_f32 v138, v138, s53, v194
	v_med3_f32 v139, v139, s53, v194
	v_pk_add_f32 v[136:137], v[136:137], 1.0 op_sel_hi:[1,0]
	v_pk_add_f32 v[138:139], v[138:139], 1.0 op_sel_hi:[1,0]
	v_pk_mul_f32 v[136:137], v[140:141], v[136:137]
	v_pk_mul_f32 v[138:139], v[142:143], v[138:139]
	v_add_f32_e32 v132, v132, v244
	v_pk_mul_f32 v[140:141], v[136:137], v[146:147]
	v_pk_mul_f32 v[136:137], v[138:139], v[148:149]
	v_min_f32_e32 v132, 0x40e00000, v132
	v_cvt_pk_bf16_f32 v137, v136, v137
	v_mul_f32_e32 v136, 0x3fd9db23, v132
	v_add_f32_e32 v134, v134, v246
	v_add_f32_e32 v135, v135, v247
	v_mul_f32_e32 v136, 0xbfb8aa3b, v136
	v_add_f32_e32 v133, v133, v245
	v_min_f32_e32 v134, 0x40e00000, v134
	v_min_f32_e32 v135, 0x40e00000, v135
	v_exp_f32_e32 v138, v136
	v_cvt_pk_bf16_f32 v136, v140, v141
	v_min_f32_e32 v133, 0x40e00000, v133
	v_mul_f32_e32 v140, 0x3fd9db23, v134
	v_mul_f32_e32 v141, 0x3fd9db23, v135
	v_mul_f32_e32 v139, 0x3fd9db23, v133
	v_mul_f32_e32 v140, 0xbfb8aa3b, v140
	v_mul_f32_e32 v141, 0xbfb8aa3b, v141
	v_mul_f32_e32 v139, 0xbfb8aa3b, v139
	v_exp_f32_e32 v140, v140
	v_exp_f32_e32 v141, v141
	v_exp_f32_e32 v139, v139
	v_add_f32_e32 v138, 1.0, v138
	v_add_f32_e32 v140, 1.0, v140
	v_add_f32_e32 v141, 1.0, v141
	v_add_f32_e32 v139, 1.0, v139
	v_add_f32_e32 v130, v130, v240
	v_rcp_f32_e32 v140, v140
	v_add_f32_e32 v131, v131, v241
	v_rcp_f32_e32 v141, v141
	v_add_f32_e32 v128, v128, v238
	v_rcp_f32_e32 v138, v138
	v_add_f32_e32 v129, v129, v239
	v_rcp_f32_e32 v139, v139
	v_med3_f32 v130, v130, s53, v194
	v_med3_f32 v131, v131, s53, v194
	v_med3_f32 v128, v128, s53, v194
	v_med3_f32 v129, v129, s53, v194
	v_pk_add_f32 v[130:131], v[130:131], 1.0 op_sel_hi:[1,0]
	v_pk_add_f32 v[128:129], v[128:129], 1.0 op_sel_hi:[1,0]
	v_pk_mul_f32 v[130:131], v[134:135], v[130:131]
	v_add_f32_e32 v124, v124, v252
	v_add_f32_e32 v125, v125, v253
	v_add_f32_e32 v126, v126, v254
	v_add_f32_e32 v127, v127, v255
	v_pk_mul_f32 v[128:129], v[132:133], v[128:129]
	v_pk_mul_f32 v[130:131], v[130:131], v[140:141]
	v_min_f32_e32 v124, 0x40e00000, v124
	v_min_f32_e32 v125, 0x40e00000, v125
	v_min_f32_e32 v126, 0x40e00000, v126
	v_min_f32_e32 v127, 0x40e00000, v127
	v_pk_mul_f32 v[128:129], v[128:129], v[138:139]
	v_cvt_pk_bf16_f32 v139, v130, v131
	v_mul_f32_e32 v130, 0x3fd9db23, v124
	v_mul_f32_e32 v131, 0x3fd9db23, v125
	v_mul_f32_e32 v132, 0x3fd9db23, v126
	v_mul_f32_e32 v133, 0x3fd9db23, v127
	v_mul_f32_e32 v130, 0xbfb8aa3b, v130
	v_mul_f32_e32 v131, 0xbfb8aa3b, v131
	v_mul_f32_e32 v132, 0xbfb8aa3b, v132
	v_mul_f32_e32 v133, 0xbfb8aa3b, v133
	v_exp_f32_e32 v130, v130
	v_exp_f32_e32 v131, v131
	v_exp_f32_e32 v132, v132
	v_exp_f32_e32 v133, v133
	v_add_f32_e32 v130, 1.0, v130
	v_add_f32_e32 v131, 1.0, v131
	v_add_f32_e32 v132, 1.0, v132
	v_add_f32_e32 v133, 1.0, v133
	v_add_f32_e32 v120, v120, v248
	v_rcp_f32_e32 v130, v130
	v_add_f32_e32 v121, v121, v249
	v_rcp_f32_e32 v131, v131
	v_add_f32_e32 v122, v122, v250
	v_rcp_f32_e32 v132, v132
	v_add_f32_e32 v123, v123, v251
	v_rcp_f32_e32 v133, v133
	v_med3_f32 v120, v120, s53, v194
	v_med3_f32 v121, v121, s53, v194
	v_med3_f32 v122, v122, s53, v194
	v_med3_f32 v123, v123, s53, v194
	v_pk_add_f32 v[120:121], v[120:121], 1.0 op_sel_hi:[1,0]
	v_pk_add_f32 v[122:123], v[122:123], 1.0 op_sel_hi:[1,0]
	v_pk_mul_f32 v[120:121], v[124:125], v[120:121]
	v_pk_mul_f32 v[122:123], v[126:127], v[122:123]
	v_add_f32_e32 v112, v112, v244
	v_pk_mul_f32 v[124:125], v[120:121], v[130:131]
	v_pk_mul_f32 v[120:121], v[122:123], v[132:133]
	v_min_f32_e32 v112, 0x40e00000, v112
	v_cvt_pk_bf16_f32 v121, v120, v121
	v_mul_f32_e32 v120, 0x3fd9db23, v112
	v_add_f32_e32 v114, v114, v246
	v_add_f32_e32 v115, v115, v247
	v_mul_f32_e32 v120, 0xbfb8aa3b, v120
	v_add_f32_e32 v113, v113, v245
	v_min_f32_e32 v114, 0x40e00000, v114
	v_min_f32_e32 v115, 0x40e00000, v115
	v_exp_f32_e32 v122, v120
	v_cvt_pk_bf16_f32 v120, v124, v125
	v_min_f32_e32 v113, 0x40e00000, v113
	v_mul_f32_e32 v124, 0x3fd9db23, v114
	v_mul_f32_e32 v125, 0x3fd9db23, v115
	v_mul_f32_e32 v123, 0x3fd9db23, v113
	v_mul_f32_e32 v124, 0xbfb8aa3b, v124
	v_mul_f32_e32 v125, 0xbfb8aa3b, v125
	v_mul_f32_e32 v123, 0xbfb8aa3b, v123
	v_exp_f32_e32 v124, v124
	v_exp_f32_e32 v125, v125
	v_exp_f32_e32 v123, v123
	v_add_f32_e32 v122, 1.0, v122
	v_add_f32_e32 v124, 1.0, v124
	v_add_f32_e32 v125, 1.0, v125
	v_add_f32_e32 v123, 1.0, v123
	v_add_f32_e32 v118, v118, v240
	v_rcp_f32_e32 v124, v124
	v_add_f32_e32 v119, v119, v241
	v_rcp_f32_e32 v125, v125
	v_add_f32_e32 v116, v116, v238
	v_rcp_f32_e32 v122, v122
	v_add_f32_e32 v117, v117, v239
	v_rcp_f32_e32 v123, v123
	v_med3_f32 v118, v118, s53, v194
	v_med3_f32 v119, v119, s53, v194
	v_med3_f32 v116, v116, s53, v194
	v_med3_f32 v117, v117, s53, v194
	v_pk_add_f32 v[118:119], v[118:119], 1.0 op_sel_hi:[1,0]
	v_pk_add_f32 v[116:117], v[116:117], 1.0 op_sel_hi:[1,0]
	v_pk_mul_f32 v[114:115], v[114:115], v[118:119]
	v_add_f32_e32 v108, v108, v252
	v_add_f32_e32 v109, v109, v253
	v_add_f32_e32 v110, v110, v254
	v_add_f32_e32 v111, v111, v255
	v_pk_mul_f32 v[112:113], v[112:113], v[116:117]
	v_pk_mul_f32 v[114:115], v[114:115], v[124:125]
	v_min_f32_e32 v108, 0x40e00000, v108
	v_min_f32_e32 v109, 0x40e00000, v109
	v_min_f32_e32 v110, 0x40e00000, v110
	v_min_f32_e32 v111, 0x40e00000, v111
	v_pk_mul_f32 v[112:113], v[112:113], v[122:123]
	v_cvt_pk_bf16_f32 v123, v114, v115
	v_mul_f32_e32 v114, 0x3fd9db23, v108
	v_mul_f32_e32 v115, 0x3fd9db23, v109
	v_mul_f32_e32 v116, 0x3fd9db23, v110
	v_mul_f32_e32 v117, 0x3fd9db23, v111
	v_mul_f32_e32 v114, 0xbfb8aa3b, v114
	v_mul_f32_e32 v115, 0xbfb8aa3b, v115
	v_mul_f32_e32 v116, 0xbfb8aa3b, v116
	v_mul_f32_e32 v117, 0xbfb8aa3b, v117
	v_exp_f32_e32 v114, v114
	v_exp_f32_e32 v115, v115
	v_exp_f32_e32 v116, v116
	v_exp_f32_e32 v117, v117
	v_add_f32_e32 v114, 1.0, v114
	v_add_f32_e32 v115, 1.0, v115
	v_add_f32_e32 v116, 1.0, v116
	v_add_f32_e32 v117, 1.0, v117
	v_add_f32_e32 v104, v104, v248
	v_rcp_f32_e32 v114, v114
	v_add_f32_e32 v105, v105, v249
	v_rcp_f32_e32 v115, v115
	v_add_f32_e32 v106, v106, v250
	v_rcp_f32_e32 v116, v116
	v_add_f32_e32 v107, v107, v251
	v_rcp_f32_e32 v117, v117
	v_med3_f32 v104, v104, s53, v194
	v_med3_f32 v105, v105, s53, v194
	v_med3_f32 v106, v106, s53, v194
	v_med3_f32 v107, v107, s53, v194
	v_pk_add_f32 v[104:105], v[104:105], 1.0 op_sel_hi:[1,0]
	v_pk_add_f32 v[106:107], v[106:107], 1.0 op_sel_hi:[1,0]
	v_pk_mul_f32 v[104:105], v[108:109], v[104:105]
	v_pk_mul_f32 v[106:107], v[110:111], v[106:107]
	v_add_f32_e32 v100, v100, v244
	v_pk_mul_f32 v[108:109], v[104:105], v[114:115]
	v_pk_mul_f32 v[104:105], v[106:107], v[116:117]
	v_min_f32_e32 v100, 0x40e00000, v100
	v_cvt_pk_bf16_f32 v105, v104, v105
	v_mul_f32_e32 v104, 0x3fd9db23, v100
	v_add_f32_e32 v102, v102, v246
	v_add_f32_e32 v103, v103, v247
	v_mul_f32_e32 v104, 0xbfb8aa3b, v104
	v_add_f32_e32 v101, v101, v245
	v_min_f32_e32 v102, 0x40e00000, v102
	v_min_f32_e32 v103, 0x40e00000, v103
	v_exp_f32_e32 v106, v104
	v_cvt_pk_bf16_f32 v104, v108, v109
	v_min_f32_e32 v101, 0x40e00000, v101
	v_mul_f32_e32 v108, 0x3fd9db23, v102
	v_mul_f32_e32 v109, 0x3fd9db23, v103
	v_mul_f32_e32 v107, 0x3fd9db23, v101
	v_mul_f32_e32 v108, 0xbfb8aa3b, v108
	v_mul_f32_e32 v109, 0xbfb8aa3b, v109
	v_mul_f32_e32 v107, 0xbfb8aa3b, v107
	v_exp_f32_e32 v108, v108
	v_exp_f32_e32 v109, v109
	v_exp_f32_e32 v107, v107
	v_add_f32_e32 v106, 1.0, v106
	v_add_f32_e32 v108, 1.0, v108
	v_add_f32_e32 v109, 1.0, v109
	v_add_f32_e32 v107, 1.0, v107
	v_add_f32_e32 v98, v98, v240
	v_rcp_f32_e32 v108, v108
	v_add_f32_e32 v99, v99, v241
	v_rcp_f32_e32 v109, v109
	v_add_f32_e32 v96, v96, v238
	v_rcp_f32_e32 v106, v106
	v_add_f32_e32 v97, v97, v239
	v_rcp_f32_e32 v107, v107
	v_med3_f32 v98, v98, s53, v194
	v_med3_f32 v99, v99, s53, v194
	v_med3_f32 v96, v96, s53, v194
	v_med3_f32 v97, v97, s53, v194
	v_pk_add_f32 v[98:99], v[98:99], 1.0 op_sel_hi:[1,0]
	v_pk_add_f32 v[96:97], v[96:97], 1.0 op_sel_hi:[1,0]
	v_pk_mul_f32 v[98:99], v[102:103], v[98:99]
	v_add_f32_e32 v92, v92, v252
	v_add_f32_e32 v93, v93, v253
	v_add_f32_e32 v94, v94, v254
	v_add_f32_e32 v95, v95, v255
	v_pk_mul_f32 v[96:97], v[100:101], v[96:97]
	v_pk_mul_f32 v[98:99], v[98:99], v[108:109]
	v_min_f32_e32 v92, 0x40e00000, v92
	v_min_f32_e32 v93, 0x40e00000, v93
	v_min_f32_e32 v94, 0x40e00000, v94
	v_min_f32_e32 v95, 0x40e00000, v95
	v_pk_mul_f32 v[96:97], v[96:97], v[106:107]
	v_cvt_pk_bf16_f32 v107, v98, v99
	v_mul_f32_e32 v98, 0x3fd9db23, v92
	v_mul_f32_e32 v99, 0x3fd9db23, v93
	v_mul_f32_e32 v100, 0x3fd9db23, v94
	v_mul_f32_e32 v101, 0x3fd9db23, v95
	v_mul_f32_e32 v98, 0xbfb8aa3b, v98
	v_mul_f32_e32 v99, 0xbfb8aa3b, v99
	v_mul_f32_e32 v100, 0xbfb8aa3b, v100
	v_mul_f32_e32 v101, 0xbfb8aa3b, v101
	v_exp_f32_e32 v98, v98
	v_exp_f32_e32 v99, v99
	v_exp_f32_e32 v100, v100
	v_exp_f32_e32 v101, v101
	v_add_f32_e32 v98, 1.0, v98
	v_add_f32_e32 v99, 1.0, v99
	v_add_f32_e32 v100, 1.0, v100
	v_add_f32_e32 v101, 1.0, v101
	v_add_f32_e32 v88, v88, v248
	v_rcp_f32_e32 v98, v98
	v_add_f32_e32 v89, v89, v249
	v_rcp_f32_e32 v99, v99
	v_add_f32_e32 v90, v90, v250
	v_rcp_f32_e32 v100, v100
	v_add_f32_e32 v91, v91, v251
	v_rcp_f32_e32 v101, v101
	v_med3_f32 v88, v88, s53, v194
	v_med3_f32 v89, v89, s53, v194
	v_med3_f32 v90, v90, s53, v194
	v_med3_f32 v91, v91, s53, v194
	v_pk_add_f32 v[88:89], v[88:89], 1.0 op_sel_hi:[1,0]
	v_pk_add_f32 v[90:91], v[90:91], 1.0 op_sel_hi:[1,0]
	v_pk_mul_f32 v[88:89], v[92:93], v[88:89]
	v_pk_mul_f32 v[90:91], v[94:95], v[90:91]
	v_add_f32_e32 v80, v80, v244
	v_pk_mul_f32 v[92:93], v[88:89], v[98:99]
	v_pk_mul_f32 v[88:89], v[90:91], v[100:101]
	v_min_f32_e32 v80, 0x40e00000, v80
	v_cvt_pk_bf16_f32 v89, v88, v89
	v_mul_f32_e32 v88, 0x3fd9db23, v80
	v_add_f32_e32 v82, v82, v246
	v_add_f32_e32 v83, v83, v247
	v_mul_f32_e32 v88, 0xbfb8aa3b, v88
	v_add_f32_e32 v81, v81, v245
	v_min_f32_e32 v82, 0x40e00000, v82
	v_min_f32_e32 v83, 0x40e00000, v83
	v_exp_f32_e32 v90, v88
	v_cvt_pk_bf16_f32 v88, v92, v93
	v_min_f32_e32 v81, 0x40e00000, v81
	v_mul_f32_e32 v92, 0x3fd9db23, v82
	v_mul_f32_e32 v93, 0x3fd9db23, v83
	v_mul_f32_e32 v91, 0x3fd9db23, v81
	v_mul_f32_e32 v92, 0xbfb8aa3b, v92
	v_mul_f32_e32 v93, 0xbfb8aa3b, v93
	v_mul_f32_e32 v91, 0xbfb8aa3b, v91
	v_exp_f32_e32 v92, v92
	v_exp_f32_e32 v93, v93
	v_exp_f32_e32 v91, v91
	v_add3_u32 v180, s68, 16, v178
	v_ashrrev_i32_e32 v181, 31, v180
	v_lshlrev_b64 v[180:181], 12, v[180:181]
	v_add_f32_e32 v92, 1.0, v92
	v_add_f32_e32 v93, 1.0, v93
	v_lshl_add_u64 v[180:181], s[50:51], 0, v[180:181]
	v_add_f32_e32 v90, 1.0, v90
	v_add_f32_e32 v91, 1.0, v91
	v_add_f32_e32 v86, v86, v240
	v_rcp_f32_e32 v92, v92
	v_add_f32_e32 v87, v87, v241
	v_rcp_f32_e32 v93, v93
	v_cvt_pk_bf16_f32 v170, v160, v161
	v_lshl_add_u64 v[160:161], v[180:181], 0, v[176:177]
	v_add_f32_e32 v84, v84, v238
	v_rcp_f32_e32 v90, v90
	v_add_f32_e32 v85, v85, v239
	v_rcp_f32_e32 v91, v91
	v_med3_f32 v86, v86, s53, v194
	v_med3_f32 v87, v87, s53, v194
	global_store_dwordx4 v[160:161], v[168:171], off
	v_add3_u32 v160, s68, 32, v178
	v_med3_f32 v84, v84, s53, v194
	v_med3_f32 v85, v85, s53, v194
	v_pk_add_f32 v[86:87], v[86:87], 1.0 op_sel_hi:[1,0]
	v_ashrrev_i32_e32 v161, 31, v160
	v_pk_add_f32 v[84:85], v[84:85], 1.0 op_sel_hi:[1,0]
	v_pk_mul_f32 v[82:83], v[82:83], v[86:87]
	v_add_f32_e32 v76, v76, v252
	v_add_f32_e32 v77, v77, v253
	v_add_f32_e32 v78, v78, v254
	v_add_f32_e32 v79, v79, v255
	v_lshlrev_b64 v[160:161], 12, v[160:161]
	v_pk_mul_f32 v[80:81], v[80:81], v[84:85]
	v_pk_mul_f32 v[82:83], v[82:83], v[92:93]
	v_min_f32_e32 v76, 0x40e00000, v76
	v_min_f32_e32 v77, 0x40e00000, v77
	v_min_f32_e32 v78, 0x40e00000, v78
	v_min_f32_e32 v79, 0x40e00000, v79
	v_add_f32_e32 v52, v52, v252
	v_add_f32_e32 v36, v36, v244
	v_lshl_add_u64 v[160:161], s[50:51], 0, v[160:161]
	v_pk_mul_f32 v[80:81], v[80:81], v[90:91]
	v_cvt_pk_bf16_f32 v91, v82, v83
	v_mul_f32_e32 v82, 0x3fd9db23, v76
	v_mul_f32_e32 v83, 0x3fd9db23, v77
	v_mul_f32_e32 v84, 0x3fd9db23, v78
	v_mul_f32_e32 v85, 0x3fd9db23, v79
	v_min_f32_e32 v52, 0x40e00000, v52
	v_min_f32_e32 v36, 0x40e00000, v36
	v_cvt_pk_bf16_f32 v154, v144, v145
	v_lshl_add_u64 v[144:145], v[160:161], 0, v[176:177]
	v_mul_f32_e32 v82, 0xbfb8aa3b, v82
	v_mul_f32_e32 v83, 0xbfb8aa3b, v83
	v_mul_f32_e32 v84, 0xbfb8aa3b, v84
	v_mul_f32_e32 v85, 0xbfb8aa3b, v85
	v_add_f32_e32 v68, v68, v244
	v_mul_f32_e32 v60, 0x3fd9db23, v52
	v_mul_f32_e32 v44, 0x3fd9db23, v36
	global_store_dwordx4 v[144:145], v[152:155], off
	v_add3_u32 v144, s68, 48, v178
	v_exp_f32_e32 v82, v82
	v_exp_f32_e32 v83, v83
	v_exp_f32_e32 v84, v84
	v_exp_f32_e32 v85, v85
	v_mul_f32_e32 v60, 0xbfb8aa3b, v60
	v_mul_f32_e32 v44, 0xbfb8aa3b, v44
	v_ashrrev_i32_e32 v145, 31, v144
	v_exp_f32_e32 v60, v60
	v_exp_f32_e32 v44, v44
	v_lshlrev_b64 v[144:145], 12, v[144:145]
	v_lshl_add_u64 v[144:145], s[50:51], 0, v[144:145]
	v_add_f32_e32 v53, v53, v253
	v_add_f32_e32 v37, v37, v245
	v_cvt_pk_bf16_f32 v138, v128, v129
	v_lshl_add_u64 v[128:129], v[144:145], 0, v[176:177]
	v_add_f32_e32 v82, 1.0, v82
	v_add_f32_e32 v83, 1.0, v83
	v_add_f32_e32 v84, 1.0, v84
	v_add_f32_e32 v85, 1.0, v85
	v_min_f32_e32 v53, 0x40e00000, v53
	v_min_f32_e32 v37, 0x40e00000, v37
	global_store_dwordx4 v[128:129], v[136:139], off
	v_add3_u32 v128, s68, 64, v178
	v_add_f32_e32 v72, v72, v248
	v_rcp_f32_e32 v82, v82
	v_add_f32_e32 v73, v73, v249
	v_rcp_f32_e32 v83, v83
	v_add_f32_e32 v74, v74, v250
	v_rcp_f32_e32 v84, v84
	v_add_f32_e32 v75, v75, v251
	v_rcp_f32_e32 v85, v85
	v_add_f32_e32 v64, v64, v238
	v_add_f32_e32 v48, v48, v248
	v_add_f32_e32 v56, 1.0, v60
	v_mul_f32_e32 v60, 0x3fd9db23, v53
	v_add_f32_e32 v32, v32, v238
	v_add_f32_e32 v40, 1.0, v44
	v_mul_f32_e32 v44, 0x3fd9db23, v37
	v_ashrrev_i32_e32 v129, 31, v128
	v_med3_f32 v72, v72, s53, v194
	v_med3_f32 v73, v73, s53, v194
	v_med3_f32 v74, v74, s53, v194
	v_med3_f32 v75, v75, s53, v194
	v_mul_f32_e32 v60, 0xbfb8aa3b, v60
	v_mul_f32_e32 v44, 0xbfb8aa3b, v44
	v_lshlrev_b64 v[128:129], 12, v[128:129]
	v_pk_add_f32 v[72:73], v[72:73], 1.0 op_sel_hi:[1,0]
	v_pk_add_f32 v[74:75], v[74:75], 1.0 op_sel_hi:[1,0]
	v_exp_f32_e32 v60, v60
	v_exp_f32_e32 v44, v44
	v_lshl_add_u64 v[128:129], s[50:51], 0, v[128:129]
	v_pk_mul_f32 v[74:75], v[78:79], v[74:75]
	v_pk_mul_f32 v[72:73], v[76:77], v[72:73]
	v_cvt_pk_bf16_f32 v122, v112, v113
	v_lshl_add_u64 v[112:113], v[128:129], 0, v[176:177]
	v_pk_mul_f32 v[76:77], v[72:73], v[82:83]
	v_pk_mul_f32 v[72:73], v[74:75], v[84:85]
	v_min_f32_e32 v68, 0x40e00000, v68
	v_add_f32_e32 v54, v54, v254
	v_add_f32_e32 v38, v38, v246
	global_store_dwordx4 v[112:113], v[120:123], off
	v_add_u32_e32 v112, s16, v178
	v_cvt_pk_bf16_f32 v73, v72, v73
	v_mul_f32_e32 v72, 0x3fd9db23, v68
	v_add_f32_e32 v69, v69, v245
	v_add_f32_e32 v70, v70, v246
	v_add_f32_e32 v71, v71, v247
	v_min_f32_e32 v54, 0x40e00000, v54
	v_min_f32_e32 v38, 0x40e00000, v38
	v_ashrrev_i32_e32 v113, 31, v112
	v_mul_f32_e32 v72, 0xbfb8aa3b, v72
	v_min_f32_e32 v69, 0x40e00000, v69
	v_add_f32_e32 v65, v65, v239
	v_min_f32_e32 v70, 0x40e00000, v70
	v_min_f32_e32 v71, 0x40e00000, v71
	v_add_f32_e32 v49, v49, v249
	v_add_f32_e32 v57, 1.0, v60
	v_mul_f32_e32 v60, 0x3fd9db23, v54
	v_add_f32_e32 v33, v33, v239
	v_add_f32_e32 v41, 1.0, v44
	v_mul_f32_e32 v44, 0x3fd9db23, v38
	v_lshlrev_b64 v[112:113], 12, v[112:113]
	v_exp_f32_e32 v74, v72
	v_cvt_pk_bf16_f32 v72, v76, v77
	v_mul_f32_e32 v75, 0x3fd9db23, v69
	v_mul_f32_e32 v76, 0x3fd9db23, v70
	v_mul_f32_e32 v77, 0x3fd9db23, v71
	v_mul_f32_e32 v60, 0xbfb8aa3b, v60
	v_mul_f32_e32 v44, 0xbfb8aa3b, v44
	v_lshl_add_u64 v[112:113], s[50:51], 0, v[112:113]
	v_mul_f32_e32 v75, 0xbfb8aa3b, v75
	v_mul_f32_e32 v76, 0xbfb8aa3b, v76
	v_mul_f32_e32 v77, 0xbfb8aa3b, v77
	v_exp_f32_e32 v60, v60
	v_exp_f32_e32 v44, v44
	v_cvt_pk_bf16_f32 v106, v96, v97
	v_lshl_add_u64 v[96:97], v[112:113], 0, v[176:177]
	s_add_i32 s16, s68, 0x60
	v_exp_f32_e32 v75, v75
	v_exp_f32_e32 v76, v76
	v_exp_f32_e32 v77, v77
	global_store_dwordx4 v[96:97], v[104:107], off
	v_add_u32_e32 v96, s16, v178
	v_add_f32_e32 v55, v55, v255
	v_add_f32_e32 v39, v39, v247
	v_ashrrev_i32_e32 v97, 31, v96
	v_min_f32_e32 v55, 0x40e00000, v55
	v_min_f32_e32 v39, 0x40e00000, v39
	v_lshlrev_b64 v[96:97], 12, v[96:97]
	v_add_f32_e32 v66, v66, v240
	v_add_f32_e32 v50, v50, v250
	v_add_f32_e32 v58, 1.0, v60
	v_mul_f32_e32 v60, 0x3fd9db23, v55
	v_add_f32_e32 v34, v34, v240
	v_add_f32_e32 v42, 1.0, v44
	v_mul_f32_e32 v44, 0x3fd9db23, v39
	v_lshl_add_u64 v[96:97], s[50:51], 0, v[96:97]
	v_add_f32_e32 v74, 1.0, v74
	v_add_f32_e32 v75, 1.0, v75
	v_add_f32_e32 v76, 1.0, v76
	v_add_f32_e32 v77, 1.0, v77
	v_mul_f32_e32 v60, 0xbfb8aa3b, v60
	v_mul_f32_e32 v44, 0xbfb8aa3b, v44
	v_cvt_pk_bf16_f32 v90, v80, v81
	v_lshl_add_u64 v[80:81], v[96:97], 0, v[176:177]
	s_add_i32 s16, s68, 0x70
	v_rcp_f32_e32 v74, v74
	v_rcp_f32_e32 v75, v75
	v_rcp_f32_e32 v76, v76
	v_add_f32_e32 v67, v67, v241
	v_rcp_f32_e32 v77, v77
	v_exp_f32_e32 v60, v60
	v_exp_f32_e32 v44, v44
	global_store_dwordx4 v[80:81], v[88:91], off
	v_add_u32_e32 v80, s16, v178
	v_med3_f32 v64, v64, s53, v194
	v_med3_f32 v65, v65, s53, v194
	v_med3_f32 v66, v66, s53, v194
	v_med3_f32 v67, v67, s53, v194
	v_ashrrev_i32_e32 v81, 31, v80
	v_pk_add_f32 v[64:65], v[64:65], 1.0 op_sel_hi:[1,0]
	v_pk_add_f32 v[66:67], v[66:67], 1.0 op_sel_hi:[1,0]
	v_lshlrev_b64 v[80:81], 12, v[80:81]
	v_pk_mul_f32 v[66:67], v[70:71], v[66:67]
	v_pk_mul_f32 v[64:65], v[68:69], v[64:65]
	v_lshl_add_u64 v[80:81], s[50:51], 0, v[80:81]
	v_pk_mul_f32 v[64:65], v[64:65], v[74:75]
	v_pk_mul_f32 v[66:67], v[66:67], v[76:77]
	v_add_f32_e32 v51, v51, v251
	v_add_f32_e32 v59, 1.0, v60
	v_add_f32_e32 v35, v35, v241
	v_add_f32_e32 v43, 1.0, v44
	v_cvt_pk_bf16_f32 v75, v66, v67
	v_cvt_pk_bf16_f32 v74, v64, v65
	v_lshl_add_u64 v[64:65], v[80:81], 0, v[176:177]
	s_add_i32 s16, s68, 0x80
	v_rcp_f32_e32 v56, v56
	v_rcp_f32_e32 v57, v57
	v_rcp_f32_e32 v58, v58
	v_rcp_f32_e32 v59, v59
	v_rcp_f32_e32 v40, v40
	v_rcp_f32_e32 v41, v41
	v_rcp_f32_e32 v42, v42
	v_rcp_f32_e32 v43, v43
	global_store_dwordx4 v[64:65], v[72:75], off
	v_add_u32_e32 v64, s16, v178
	v_med3_f32 v48, v48, s53, v194
	v_med3_f32 v49, v49, s53, v194
	v_med3_f32 v50, v50, s53, v194
	v_med3_f32 v51, v51, s53, v194
	v_med3_f32 v32, v32, s53, v194
	v_med3_f32 v33, v33, s53, v194
	v_med3_f32 v34, v34, s53, v194
	v_med3_f32 v35, v35, s53, v194
	v_ashrrev_i32_e32 v65, 31, v64
	v_pk_add_f32 v[48:49], v[48:49], 1.0 op_sel_hi:[1,0]
	v_pk_add_f32 v[50:51], v[50:51], 1.0 op_sel_hi:[1,0]
	v_pk_add_f32 v[32:33], v[32:33], 1.0 op_sel_hi:[1,0]
	v_pk_add_f32 v[34:35], v[34:35], 1.0 op_sel_hi:[1,0]
	v_lshlrev_b64 v[64:65], 12, v[64:65]
	v_pk_mul_f32 v[50:51], v[54:55], v[50:51]
	v_pk_mul_f32 v[48:49], v[52:53], v[48:49]
	v_pk_mul_f32 v[34:35], v[38:39], v[34:35]
	v_pk_mul_f32 v[32:33], v[36:37], v[32:33]
	v_lshl_add_u64 v[64:65], s[50:51], 0, v[64:65]
	v_pk_mul_f32 v[52:53], v[48:49], v[56:57]
	v_pk_mul_f32 v[48:49], v[50:51], v[58:59]
	v_pk_mul_f32 v[32:33], v[32:33], v[40:41]
	v_pk_mul_f32 v[34:35], v[34:35], v[42:43]
	v_cvt_pk_bf16_f32 v49, v48, v49
	v_cvt_pk_bf16_f32 v48, v52, v53
	v_cvt_pk_bf16_f32 v51, v34, v35
	v_cvt_pk_bf16_f32 v50, v32, v33
	v_lshl_add_u64 v[32:33], v[64:65], 0, v[176:177]
	s_mov_b32 s68, s43
	global_store_dwordx4 v[32:33], v[48:51], off
	s_cbranch_vccnz .LBB0_663
